# baseline (speedup 1.0000x reference)
_Z6k_gramILi0EEvPK15HIP_vector_typeIjLj4EEPyPf:
	s_load_dwordx4 s[8:11], s[0:1], 0x0
	s_load_dwordx2 s[4:5], s[0:1], 0x10
	s_lshl_b32 s0, s2, 2
	s_and_b32 s0, s0, 28
	s_ashr_i32 s1, s2, 6
	s_add_i32 s16, s0, s1
	v_readfirstlane_b32 s23, v0
	s_ashr_i32 s17, s16, 31
	s_lshr_b32 s21, s23, 6
	s_bfe_u32 s18, s23, 0x20006
	s_lshr_b32 s22, s2, 3
	s_bfe_u32 s20, s2, 0x30003
	s_lshl_b64 s[0:1], s[16:17], 20
	s_waitcnt lgkmcnt(0)
	s_add_u32 s12, s8, s0
	v_mov_b32_e32 v1, 0x20000
	s_addc_u32 s0, s9, s1
	s_lshl_b32 s1, s20, 2
	v_lshl_or_b32 v1, v0, 2, v1
	v_bfrev_b32_e32 v2, 1
	s_cmp_lt_u32 s20, 4
	ds_write_b32 v1, v2
	s_mov_b32 s24, 4
	s_mov_b32 s15, 0x20000
	s_and_b32 s13, s0, 0xffff
	s_mov_b32 s14, 0x100000
	v_lshlrev_b32_e32 v166, 4, v0
	s_lshl_b32 s25, s21, 10
	s_lshl_b32 s0, s20, 17
	s_mov_b32 m0, s25
	s_nop 0
	buffer_load_dwordx4 v166, s[12:15], s0 offen lds
	s_add_i32 s26, s25, 0x2000
	s_or_b32 s2, s0, 0x2000
	s_mov_b32 m0, s26
	s_nop 0
	buffer_load_dwordx4 v166, s[12:15], s2 offen lds
	s_add_i32 s27, s25, 0x4000
	s_or_b32 s2, s0, 0x8000
	s_mov_b32 m0, s27
	s_nop 0
	buffer_load_dwordx4 v166, s[12:15], s2 offen lds
	s_add_i32 s28, s25, 0x6000
	s_or_b32 s2, s0, 0xa000
	s_mov_b32 m0, s28
	s_nop 0
	buffer_load_dwordx4 v166, s[12:15], s2 offen lds
	s_add_i32 s34, s25, 0x10000
	s_or_b32 s2, s0, 0x10000
	s_mov_b32 m0, s34
	s_nop 0
	buffer_load_dwordx4 v166, s[12:15], s2 offen lds
	s_add_i32 s35, s25, 0x12000
	s_or_b32 s2, s0, 0x12000
	s_mov_b32 m0, s35
	s_nop 0
	buffer_load_dwordx4 v166, s[12:15], s2 offen lds
	s_add_i32 s36, s25, 0x14000
	s_or_b32 s2, s0, 0x18000
	s_mov_b32 m0, s36
	s_nop 0
	buffer_load_dwordx4 v166, s[12:15], s2 offen lds
	s_add_i32 s37, s25, 0x16000
	s_or_b32 s2, s0, 0x1a000
	s_mov_b32 m0, s37
	s_nop 0
	buffer_load_dwordx4 v166, s[12:15], s2 offen lds
	s_add_i32 s29, s25, 0x8000
	s_or_b32 s2, s0, 0x4000
	s_mov_b32 m0, s29
	s_nop 0
	buffer_load_dwordx4 v166, s[12:15], s2 offen lds
	s_add_i32 s30, s25, 0xa000
	s_or_b32 s2, s0, 0x6000
	s_mov_b32 m0, s30
	s_nop 0
	buffer_load_dwordx4 v166, s[12:15], s2 offen lds
	s_add_i32 s31, s25, 0xc000
	s_or_b32 s2, s0, 0xc000
	s_mov_b32 m0, s31
	s_nop 0
	buffer_load_dwordx4 v166, s[12:15], s2 offen lds
	s_add_i32 s33, s25, 0xe000
	s_or_b32 s2, s0, 0xe000
	s_mov_b32 m0, s33
	s_nop 0
	buffer_load_dwordx4 v166, s[12:15], s2 offen lds
	s_add_i32 s38, s25, 0x18000
	s_or_b32 s2, s0, 0x14000
	s_mov_b32 m0, s38
	s_nop 0
	buffer_load_dwordx4 v166, s[12:15], s2 offen lds
	s_add_i32 s39, s25, 0x1a000
	s_or_b32 s2, s0, 0x16000
	s_mov_b32 m0, s39
	s_nop 0
	buffer_load_dwordx4 v166, s[12:15], s2 offen lds
	s_add_i32 s40, s25, 0x1c000
	s_or_b32 s2, s0, 0x1c000
	s_mov_b32 m0, s40
	s_nop 0
	buffer_load_dwordx4 v166, s[12:15], s2 offen lds
	s_add_i32 s42, s25, 0x1e000
	s_or_b32 s2, s0, 0x1e000
	s_mov_b32 m0, s42
	s_nop 0
	buffer_load_dwordx4 v166, s[12:15], s2 offen lds
	s_lshl_b32 s0, s23, 9
	s_lshl_b32 s2, s23, 8
	v_and_b32_e32 v167, 15, v0
	v_bfe_u32 v160, v0, 4, 2
	s_and_b32 s0, s0, 0x10000
	s_and_b32 s2, s2, 0x4000
	v_lshlrev_b32_e32 v128, 9, v160
	v_lshlrev_b32_e32 v129, 4, v167
	s_or_b32 s0, s0, s2
	v_or3_b32 v124, s0, v128, v129
	s_waitcnt vmcnt(8)
	s_waitcnt lgkmcnt(0)
	s_barrier
	ds_read_b128 v[0:3], v124
	ds_read_b128 v[4:7], v124 offset:256
	ds_read_b128 v[8:11], v124 offset:2048
	ds_read_b128 v[12:15], v124 offset:2304
	ds_read_b128 v[16:19], v124 offset:4096
	ds_read_b128 v[20:23], v124 offset:4352
	ds_read_b128 v[24:27], v124 offset:6144
	ds_read_b128 v[28:31], v124 offset:6400
	ds_read_b128 v[32:35], v124 offset:8192
	ds_read_b128 v[36:39], v124 offset:8448
	ds_read_b128 v[40:43], v124 offset:10240
	ds_read_b128 v[44:47], v124 offset:10496
	ds_read_b128 v[48:51], v124 offset:12288
	ds_read_b128 v[52:55], v124 offset:12544
	ds_read_b128 v[56:59], v124 offset:14336
	ds_read_b128 v[60:63], v124 offset:14592
	s_lshr_b32 s41, s23, 8
	s_lshl_b32 s0, s41, 14
	s_lshl_b32 s50, s24, 2
	v_or3_b32 v168, s0, v128, v129
	s_or_b32 s43, s18, s1
	s_lshl_b32 s0, s16, 10
	s_lshl_b32 s1, s43, 5
	ds_read_b128 v[128:131], v168
	ds_read_b128 v[132:135], v168 offset:256
	ds_read_b128 v[136:139], v168 offset:2048
	ds_read_b128 v[140:143], v168 offset:2304
	s_or_b32 s0, s1, s0
	v_or_b32_e32 v144, s0, v167
	v_lshlrev_b32_e32 v146, 2, v160
	v_ashrrev_i32_e32 v145, 31, v144
	v_lshl_add_u64 v[164:165], v[144:145], 2, s[4:5]
	v_or_b32_e32 v144, 1, v146
	v_cmp_eq_u32_e64 s[2:3], v144, v167
	v_or_b32_e32 v144, 2, v146
	s_waitcnt vmcnt(8)
	v_cmp_eq_u32_e64 s[4:5], v144, v167
	v_or_b32_e32 v144, 3, v146
	s_add_i32 s44, s50, 3
	s_lshl_b32 s45, s22, 2
	v_cmp_eq_u32_e64 s[0:1], v146, v167
	v_cmp_eq_u32_e64 s[6:7], v144, v167
	v_add_u32_e32 v169, 0x10000, v168
	v_add_u32_e32 v170, 0x10100, v168
	v_add_u32_e32 v171, 0x10800, v168
	v_add_u32_e32 v172, 0x10900, v168
	s_add_i32 s8, s45, 28
	s_and_b32 s8, s8, 28
	s_add_i32 s8, s41, s8
	s_lshl_b32 s8, s8, 1
	s_add_i32 s9, s8, 4
	s_add_i32 s8, s8, 5
	v_mov_b32_e32 v148, s9
	v_mov_b32_e32 v149, s8
	ds_read_b128 v[148:151], v168 offset:4096
	s_waitcnt lgkmcnt(4)
	v_mfma_f32_16x16x32_bf16 v[144:147], v[0:3], v[128:131], 0
	v_mfma_f32_16x16x32_bf16 v[128:131], v[4:7], v[128:131], 0
	ds_read_b128 v[156:159], v168 offset:4352
	s_waitcnt lgkmcnt(4)
	v_mfma_f32_16x16x32_bf16 v[152:155], v[0:3], v[132:135], 0
	v_mfma_f32_16x16x32_bf16 v[132:135], v[4:7], v[132:135], 0
	s_waitcnt lgkmcnt(3)
	v_mfma_f32_16x16x32_bf16 v[144:147], v[8:11], v[136:139], v[144:147]
	ds_read_b128 v[174:177], v168 offset:6144
	v_mfma_f32_16x16x32_bf16 v[128:131], v[12:15], v[136:139], v[128:131]
	s_waitcnt lgkmcnt(3)
	v_mfma_f32_16x16x32_bf16 v[136:139], v[8:11], v[140:143], v[152:155]
	s_nop 2
	ds_read_b128 v[152:155], v168 offset:6400
	v_mfma_f32_16x16x32_bf16 v[132:135], v[12:15], v[140:143], v[132:135]
	s_waitcnt lgkmcnt(3)
	v_mfma_f32_16x16x32_bf16 v[140:143], v[16:19], v[148:151], v[144:147]
	s_nop 2
	ds_read_b128 v[144:147], v168 offset:8192
	v_mfma_f32_16x16x32_bf16 v[128:131], v[20:23], v[148:151], v[128:131]
	ds_read_b128 v[148:151], v168 offset:8448
	s_waitcnt lgkmcnt(4)
	v_mfma_f32_16x16x32_bf16 v[136:139], v[16:19], v[156:159], v[136:139]
	v_mfma_f32_16x16x32_bf16 v[132:135], v[20:23], v[156:159], v[132:135]
	ds_read_b128 v[156:159], v168 offset:10240
	s_waitcnt lgkmcnt(4)
	v_mfma_f32_16x16x32_bf16 v[140:143], v[24:27], v[174:177], v[140:143]
	v_mfma_f32_16x16x32_bf16 v[128:131], v[28:31], v[174:177], v[128:131]
	s_waitcnt lgkmcnt(3)
	v_mfma_f32_16x16x32_bf16 v[136:139], v[24:27], v[152:155], v[136:139]
	ds_read_b128 v[174:177], v168 offset:10496
	v_mfma_f32_16x16x32_bf16 v[132:135], v[28:31], v[152:155], v[132:135]
	ds_read_b128 v[152:155], v168 offset:12288
	s_waitcnt lgkmcnt(4)
	v_mfma_f32_16x16x32_bf16 v[140:143], v[32:35], v[144:147], v[140:143]
	v_mfma_f32_16x16x32_bf16 v[128:131], v[36:39], v[144:147], v[128:131]
	ds_read_b128 v[144:147], v168 offset:12544
	s_waitcnt lgkmcnt(4)
	v_mfma_f32_16x16x32_bf16 v[136:139], v[32:35], v[148:151], v[136:139]
	v_mfma_f32_16x16x32_bf16 v[132:135], v[36:39], v[148:151], v[132:135]
	ds_read_b128 v[148:151], v168 offset:14336
	s_waitcnt lgkmcnt(4)
	v_mfma_f32_16x16x32_bf16 v[140:143], v[40:43], v[156:159], v[140:143]
	v_mfma_f32_16x16x32_bf16 v[128:131], v[44:47], v[156:159], v[128:131]
	ds_read_b128 v[156:159], v168 offset:14592
	s_waitcnt lgkmcnt(4)
	v_mfma_f32_16x16x32_bf16 v[136:139], v[40:43], v[174:177], v[136:139]
	v_mfma_f32_16x16x32_bf16 v[132:135], v[44:47], v[174:177], v[132:135]
	s_waitcnt lgkmcnt(3)
	v_mfma_f32_16x16x32_bf16 v[140:143], v[48:51], v[152:155], v[140:143]
	ds_read_b128 v[174:177], v168 offset:32768
	v_mfma_f32_16x16x32_bf16 v[128:131], v[52:55], v[152:155], v[128:131]
	ds_read_b128 v[152:155], v168 offset:33024
	s_waitcnt lgkmcnt(4)
	v_mfma_f32_16x16x32_bf16 v[136:139], v[48:51], v[144:147], v[136:139]
	v_mfma_f32_16x16x32_bf16 v[132:135], v[52:55], v[144:147], v[132:135]
	ds_read_b128 v[144:147], v168 offset:34816
	s_waitcnt lgkmcnt(4)
	v_mfma_f32_16x16x32_bf16 v[140:143], v[56:59], v[148:151], v[140:143]
	v_mfma_f32_16x16x32_bf16 v[128:131], v[60:63], v[148:151], v[128:131]
	ds_read_b128 v[148:151], v168 offset:35072
	s_waitcnt lgkmcnt(4)
	v_mfma_f32_16x16x32_bf16 v[136:139], v[56:59], v[156:159], v[136:139]
	v_mfma_f32_16x16x32_bf16 v[132:135], v[60:63], v[156:159], v[132:135]
	s_waitcnt vmcnt(0)
	s_barrier
	ds_read_b128 v[174:177], v168 offset:32768
	ds_read_b128 v[152:155], v168 offset:33024
	ds_read_b128 v[144:147], v168 offset:34816
	ds_read_b128 v[148:151], v168 offset:35072
	ds_read_b128 v[64:67], v124 offset:32768
	ds_read_b128 v[68:71], v124 offset:33024
	ds_read_b128 v[72:75], v124 offset:34816
	ds_read_b128 v[76:79], v124 offset:35072
	ds_read_b128 v[80:83], v124 offset:36864
	ds_read_b128 v[84:87], v124 offset:37120
	ds_read_b128 v[88:91], v124 offset:38912
	ds_read_b128 v[92:95], v124 offset:39168
	ds_read_b128 v[96:99], v124 offset:40960
	ds_read_b128 v[100:103], v124 offset:41216
	ds_read_b128 v[104:107], v124 offset:43008
	ds_read_b128 v[108:111], v124 offset:43264
	ds_read_b128 v[112:115], v124 offset:45056
	ds_read_b128 v[116:119], v124 offset:45312
	ds_read_b128 v[120:123], v124 offset:47104
	ds_read_b128 v[124:127], v124 offset:47360
	s_and_b32 s8, s45, 28
	s_add_i32 s8, s8, s41
	s_lshl_b32 s19, s8, 1
	s_or_b32 s51, s19, 1
	v_mov_b32_e32 v156, s51
	v_mov_b32_e32 v157, s19
	ds_read_b128 v[156:159], v168 offset:36864
	s_waitcnt lgkmcnt(4)
	v_mfma_f32_16x16x32_bf16 v[140:143], v[64:67], v[174:177], v[140:143]
	s_min_u32 s9, s44, 4
	s_add_i32 s46, s9, s45
	v_mov_b32_e32 v202, s19
	v_mfma_f32_16x16x32_bf16 v[128:131], v[68:71], v[174:177], v[128:131]
	v_mov_b32_e32 v206, s51
	s_and_b32 s46, s46, 28
	s_and_b32 s47, s9, 2
	s_lshl_b32 s9, s9, 14
	s_or_b32 s46, s47, s46
	s_and_b32 s9, s9, 0x4000
	ds_read_b128 v[174:177], v168 offset:37120
	s_waitcnt lgkmcnt(4)
	v_mfma_f32_16x16x32_bf16 v[136:139], v[64:67], v[152:155], v[136:139]
	s_lshl_b32 s46, s46, 15
	s_or_b32 s9, s46, s9
	s_mov_b32 m0, s25
	s_nop 0
	buffer_load_dwordx4 v166, s[12:15], s9 offen lds
	v_mfma_f32_16x16x32_bf16 v[132:135], v[68:71], v[152:155], v[132:135]
	ds_read_b128 v[152:155], v168 offset:38912
	s_waitcnt lgkmcnt(4)
	v_mfma_f32_16x16x32_bf16 v[140:143], v[72:75], v[144:147], v[140:143]
	v_mfma_f32_16x16x32_bf16 v[128:131], v[76:79], v[144:147], v[128:131]
	ds_read_b128 v[144:147], v168 offset:39168
	s_waitcnt lgkmcnt(4)
	v_mfma_f32_16x16x32_bf16 v[136:139], v[72:75], v[148:151], v[136:139]
	v_mfma_f32_16x16x32_bf16 v[132:135], v[76:79], v[148:151], v[132:135]
	ds_read_b128 v[148:151], v168 offset:40960
	s_waitcnt lgkmcnt(4)
	v_mfma_f32_16x16x32_bf16 v[140:143], v[80:83], v[156:159], v[140:143]
	v_mfma_f32_16x16x32_bf16 v[128:131], v[84:87], v[156:159], v[128:131]
	ds_read_b128 v[156:159], v168 offset:41216
	s_waitcnt lgkmcnt(4)
	v_mfma_f32_16x16x32_bf16 v[136:139], v[80:83], v[174:177], v[136:139]
	s_or_b32 s46, s9, 0x2000
	s_mov_b32 m0, s26
	s_nop 0
	buffer_load_dwordx4 v166, s[12:15], s46 offen lds
	v_mfma_f32_16x16x32_bf16 v[132:135], v[84:87], v[174:177], v[132:135]
	s_waitcnt lgkmcnt(3)
	v_mfma_f32_16x16x32_bf16 v[140:143], v[88:91], v[152:155], v[140:143]
	ds_read_b128 v[174:177], v168 offset:43008
	v_mfma_f32_16x16x32_bf16 v[128:131], v[92:95], v[152:155], v[128:131]
	ds_read_b128 v[152:155], v168 offset:43264
	s_waitcnt lgkmcnt(4)
	v_mfma_f32_16x16x32_bf16 v[136:139], v[88:91], v[144:147], v[136:139]
	v_mfma_f32_16x16x32_bf16 v[132:135], v[92:95], v[144:147], v[132:135]
	ds_read_b128 v[144:147], v168 offset:45056
	s_waitcnt lgkmcnt(4)
	v_mfma_f32_16x16x32_bf16 v[140:143], v[96:99], v[148:151], v[140:143]
	v_mfma_f32_16x16x32_bf16 v[128:131], v[100:103], v[148:151], v[128:131]
	ds_read_b128 v[148:151], v168 offset:45312
	s_waitcnt lgkmcnt(4)
	v_mfma_f32_16x16x32_bf16 v[136:139], v[96:99], v[156:159], v[136:139]
	s_or_b32 s46, s9, 0x8000
	s_mov_b32 m0, s27
	s_nop 0
	buffer_load_dwordx4 v166, s[12:15], s46 offen lds
	v_mfma_f32_16x16x32_bf16 v[132:135], v[100:103], v[156:159], v[132:135]
	s_waitcnt lgkmcnt(3)
	v_mfma_f32_16x16x32_bf16 v[140:143], v[104:107], v[174:177], v[140:143]
	ds_read_b128 v[178:181], v168 offset:47104
	v_mfma_f32_16x16x32_bf16 v[128:131], v[108:111], v[174:177], v[128:131]
	s_waitcnt lgkmcnt(3)
	v_mfma_f32_16x16x32_bf16 v[136:139], v[104:107], v[152:155], v[136:139]
	ds_read_b128 v[174:177], v168 offset:47360
	v_mfma_f32_16x16x32_bf16 v[132:135], v[108:111], v[152:155], v[132:135]
	ds_read_b128 v[156:159], v169
	s_waitcnt lgkmcnt(4)
	v_mfma_f32_16x16x32_bf16 v[140:143], v[112:115], v[144:147], v[140:143]
	v_mfma_f32_16x16x32_bf16 v[128:131], v[116:119], v[144:147], v[128:131]
	ds_read_b128 v[152:155], v170
	s_waitcnt lgkmcnt(4)
	v_mfma_f32_16x16x32_bf16 v[144:147], v[112:115], v[148:151], v[136:139]
	s_or_b32 s9, s9, 0xa000
	s_mov_b32 m0, s28
	s_nop 0
	buffer_load_dwordx4 v166, s[12:15], s9 offen lds
	v_mfma_f32_16x16x32_bf16 v[132:135], v[116:119], v[148:151], v[132:135]
	ds_read_b128 v[148:151], v171
	s_waitcnt lgkmcnt(4)
	v_mfma_f32_16x16x32_bf16 v[136:139], v[120:123], v[178:181], v[140:143]
	v_mfma_f32_16x16x32_bf16 v[128:131], v[124:127], v[178:181], v[128:131]
	s_waitcnt lgkmcnt(3)
	v_mfma_f32_16x16x32_bf16 v[140:143], v[120:123], v[174:177], v[144:147]
	s_nop 2
	ds_read_b128 v[144:147], v172
	v_mfma_f32_16x16x32_bf16 v[132:135], v[124:127], v[174:177], v[132:135]
	s_waitcnt vmcnt(4)
	s_barrier
	s_cmp_lg_u32 s8, s43
	s_cbranch_scc1 .LBB3_11
	s_and_saveexec_b64 s[8:9], s[0:1]
	s_cbranch_execnz .LBB3_38
	s_or_b64 exec, exec, s[8:9]
	s_and_saveexec_b64 s[8:9], s[2:3]
	s_cbranch_execnz .LBB3_39
